# v17 with the epilogue weight conversion re-mapped so each store instruction writes 64-byte contiguous pieces (4 lanes per row), stores nt
# baseline (speedup 1.0000x reference)
; #define LAS __attribute__((address_space(3)))
; DI unsigned pk_bf16(float lo, float hi) { const f32x2 v = {lo, hi}; return __builtin_bit_cast(unsigned, __builtin_convertvector(v, bf16x2_t)); }
; DI void tr_tile(const float* src, int N, int k0, int n0, float scale, bf16_t* dst_row0  , int K, bf16_t* dst_lo, LAS bf16_t* T, int lane) {
; #pragma unroll 4
;     for (int it = 0; it < 8; ++it) {
;         const int kk = it * 8 + 2 * (lane >> 4), c4 = (lane & 15) * 4;
;         const f32x4 v0 = *(const f32x4*)(src + (size_t)(k0 + kk) * N + n0 + c4) * scale, v1 = *(const f32x4*)(src + (size_t)(k0 + kk + 1) * N + n0 + c4) * scale;
; #pragma unroll
;         for (int j = 0; j < 4; ++j) *(LAS unsigned*)(T + (c4 + j) * 72 + kk) = pk_bf16(v0[j], v1[j]);
;     }
;     __builtin_amdgcn_s_waitcnt(0xc07f);
; #pragma unroll 4
;     for (int it = 0; it < 8; ++it) {
;         const int n = it * 8 + (lane >> 3), kc = (lane & 7) * 8;
;         const u32x4 w = *(const LAS u32x4*)(T + n * 72 + kc);
;         *(u32x4*)(dst_row0 + (size_t)n * K + kc) = w;
;     }
.Lcv_issue:
	s_waitcnt lgkmcnt(0)
	s_add_u32 s80, s80, s82
	s_addc_u32 s81, s81, 0
	s_add_u32 s98, s76, s83
	s_addc_u32 s99, s77, 0
	v_mbcnt_lo_u32_b32 v224, -1, 0
	v_mbcnt_hi_u32_b32 v224, -1, v224
	v_and_b32_e32 v226, 3, v224
	v_lshrrev_b32_e32 v224, 2, v224
	s_lshl_b32 s75, s84, 3
	v_mul_lo_u32 v174, v226, s75
	v_lshl_add_u32 v174, v224, 2, v174
	v_mul_lo_u32 v175, v224, s85
	v_lshl_add_u32 v175, v226, 4, v175
	s_mul_i32 s75, s84, 24
	global_load_dword v178, v174, s[80:81] nt
	global_load_dword v186, v174, s[80:81] offset:64 nt
	global_load_dword v194, v174, s[80:81] offset:128 nt
	global_load_dword v202, v174, s[80:81] offset:192 nt
	s_add_u32 s80, s80, s84
	s_addc_u32 s81, s81, 0
	global_load_dword v179, v174, s[80:81] nt
	global_load_dword v187, v174, s[80:81] offset:64 nt
	global_load_dword v195, v174, s[80:81] offset:128 nt
	global_load_dword v203, v174, s[80:81] offset:192 nt
	s_add_u32 s80, s80, s84
	s_addc_u32 s81, s81, 0
	global_load_dword v180, v174, s[80:81] nt
	global_load_dword v188, v174, s[80:81] offset:64 nt
	global_load_dword v196, v174, s[80:81] offset:128 nt
	global_load_dword v204, v174, s[80:81] offset:192 nt
	s_add_u32 s80, s80, s84
	s_addc_u32 s81, s81, 0
	global_load_dword v181, v174, s[80:81] nt
	global_load_dword v189, v174, s[80:81] offset:64 nt
	global_load_dword v197, v174, s[80:81] offset:128 nt
	global_load_dword v205, v174, s[80:81] offset:192 nt
	s_add_u32 s80, s80, s84
	s_addc_u32 s81, s81, 0
	global_load_dword v182, v174, s[80:81] nt
	global_load_dword v190, v174, s[80:81] offset:64 nt
	global_load_dword v198, v174, s[80:81] offset:128 nt
	global_load_dword v206, v174, s[80:81] offset:192 nt
	s_add_u32 s80, s80, s84
	s_addc_u32 s81, s81, 0
	global_load_dword v183, v174, s[80:81] nt
	global_load_dword v191, v174, s[80:81] offset:64 nt
	global_load_dword v199, v174, s[80:81] offset:128 nt
	global_load_dword v207, v174, s[80:81] offset:192 nt
	s_add_u32 s80, s80, s84
	s_addc_u32 s81, s81, 0
	global_load_dword v184, v174, s[80:81] nt
	global_load_dword v192, v174, s[80:81] offset:64 nt
	global_load_dword v200, v174, s[80:81] offset:128 nt
	global_load_dword v208, v174, s[80:81] offset:192 nt
	s_add_u32 s80, s80, s84
	s_addc_u32 s81, s81, 0
	global_load_dword v185, v174, s[80:81] nt
	global_load_dword v193, v174, s[80:81] offset:64 nt
	global_load_dword v201, v174, s[80:81] offset:128 nt
	global_load_dword v209, v174, s[80:81] offset:192 nt
	s_add_u32 s80, s80, s84
	s_addc_u32 s81, s81, 0
	s_add_u32 s80, s80, s75
	s_addc_u32 s81, s81, 0
	global_load_dword v210, v174, s[80:81] nt
	global_load_dword v218, v174, s[80:81] offset:64 nt
	global_load_dword v238, v174, s[80:81] offset:128 nt
	global_load_dword v246, v174, s[80:81] offset:192 nt
	s_add_u32 s80, s80, s84
	s_addc_u32 s81, s81, 0
	global_load_dword v211, v174, s[80:81] nt
	global_load_dword v219, v174, s[80:81] offset:64 nt
	global_load_dword v239, v174, s[80:81] offset:128 nt
	global_load_dword v247, v174, s[80:81] offset:192 nt
	s_add_u32 s80, s80, s84
	s_addc_u32 s81, s81, 0
	global_load_dword v212, v174, s[80:81] nt
	global_load_dword v220, v174, s[80:81] offset:64 nt
	global_load_dword v240, v174, s[80:81] offset:128 nt
	global_load_dword v248, v174, s[80:81] offset:192 nt
	s_add_u32 s80, s80, s84
	s_addc_u32 s81, s81, 0
	global_load_dword v213, v174, s[80:81] nt
	global_load_dword v221, v174, s[80:81] offset:64 nt
	global_load_dword v241, v174, s[80:81] offset:128 nt
	global_load_dword v249, v174, s[80:81] offset:192 nt
	s_add_u32 s80, s80, s84
	s_addc_u32 s81, s81, 0
	global_load_dword v214, v174, s[80:81] nt
	global_load_dword v222, v174, s[80:81] offset:64 nt
	global_load_dword v242, v174, s[80:81] offset:128 nt
	global_load_dword v250, v174, s[80:81] offset:192 nt
	s_add_u32 s80, s80, s84
	s_addc_u32 s81, s81, 0
	global_load_dword v215, v174, s[80:81] nt
	global_load_dword v223, v174, s[80:81] offset:64 nt
	global_load_dword v243, v174, s[80:81] offset:128 nt
	global_load_dword v251, v174, s[80:81] offset:192 nt
	s_add_u32 s80, s80, s84
	s_addc_u32 s81, s81, 0
	global_load_dword v216, v174, s[80:81] nt
	global_load_dword v236, v174, s[80:81] offset:64 nt
	global_load_dword v244, v174, s[80:81] offset:128 nt
	global_load_dword v252, v174, s[80:81] offset:192 nt
	s_add_u32 s80, s80, s84
	s_addc_u32 s81, s81, 0
	global_load_dword v217, v174, s[80:81] nt
	global_load_dword v237, v174, s[80:81] offset:64 nt
	global_load_dword v245, v174, s[80:81] offset:128 nt
	global_load_dword v253, v174, s[80:81] offset:192 nt
; DI unsigned pk_bf16(float lo, float hi) { const f32x2 v = {lo, hi}; return __builtin_bit_cast(unsigned, __builtin_convertvector(v, bf16x2_t)); }
; DI float silu_mul(float g, float u) { return g * sigmoidf_(g) * u; }
;     DI void operator()(const f32x4 (&acc)[2][2][4][2], const Unit& u, int wr, int wc, int fr, int fq) const {
;     ...
;         for (int ai = 0; ai < 2; ++ai)
; #pragma unroll
;             for (int m = 0; m < 4; ++m) { const int row = u.orow + ai * 128 + wr * 64 + m * 16 + fr;
;                 bf16_t* rowp = ACT + (size_t)row * 256 + col0;
;                 float v[8];
; #pragma unroll
;                 for (int n = 0; n < 2; ++n)
; #pragma unroll
;                     for (int j = 0; j < 4; ++j) v[n * 4 + j] = silu_mul(acc[ai][0][m][n][j], acc[ai][1][m][n][j]) * w8[ai][m];
;                 u32x4 w; w.x = pk_bf16(v[0], v[1]); w.y = pk_bf16(v[2], v[3]); w.z = pk_bf16(v[4], v[5]); w.w = pk_bf16(v[6], v[7]);
;                 *(u32x4*)rowp = w; }
.Lcv_ld_done:
	v_pk_mul_f32 v[116:117], v[112:113], v[150:151] op_sel_hi:[1,0]
	v_pk_mul_f32 v[112:113], v[118:119], v[126:127]
	v_pk_mul_f32 v[120:121], v[120:121], v[150:151] op_sel_hi:[1,0]
	v_pk_mul_f32 v[112:113], v[112:113], v[114:115]
	v_pk_mul_f32 v[122:123], v[122:123], v[150:151] op_sel_hi:[1,0]
	v_pk_mul_f32 v[118:119], v[112:113], v[150:151] op_sel_hi:[1,0]
	v_lshlrev_b64 v[112:113], 1, v[168:169]
	v_lshl_add_u64 v[124:125], v[152:153], 0, v[112:113]
	v_cvt_pk_bf16_f32 v114, v120, v121
	v_cvt_pk_bf16_f32 v115, v122, v123
	v_cvt_pk_bf16_f32 v116, v116, v117
	v_cvt_pk_bf16_f32 v117, v118, v119
	global_store_dwordx4 v[124:125], v[114:117], off
	v_mul_f32_e32 v118, 0xbfb8aa3b, v110
	v_mul_f32_e32 v119, 0xbfb8aa3b, v111
	v_mul_f32_e32 v116, 0xbfb8aa3b, v108
	v_mul_f32_e32 v117, 0xbfb8aa3b, v109
	v_exp_f32_e32 v116, v116
	v_exp_f32_e32 v117, v117
	v_exp_f32_e32 v118, v118
	v_exp_f32_e32 v119, v119
	v_add_f32_e32 v116, 1.0, v116
	v_add_f32_e32 v117, 1.0, v117
	v_rcp_f32_e32 v116, v116
	v_rcp_f32_e32 v117, v117
	v_add_f32_e32 v118, 1.0, v118
	v_add_f32_e32 v119, 1.0, v119
	v_rcp_f32_e32 v118, v118
	v_rcp_f32_e32 v119, v119
	v_pk_mul_f32 v[108:109], v[108:109], v[116:117]
	v_or_b32_e32 v114, 16, v137
	v_pk_mul_f32 v[104:105], v[108:109], v[104:105]
	v_pk_mul_f32 v[108:109], v[110:111], v[118:119]
	v_mul_f32_e32 v110, 0xbfb8aa3b, v102
	v_pk_mul_f32 v[106:107], v[108:109], v[106:107]
	v_mul_f32_e32 v108, 0xbfb8aa3b, v100
	v_mul_f32_e32 v109, 0xbfb8aa3b, v101
	v_exp_f32_e32 v108, v108
	v_exp_f32_e32 v109, v109
	v_mul_f32_e32 v111, 0xbfb8aa3b, v103
	v_exp_f32_e32 v110, v110
	v_exp_f32_e32 v111, v111
	v_add_f32_e32 v108, 1.0, v108
	v_add_f32_e32 v109, 1.0, v109
	v_rcp_f32_e32 v108, v108
	v_rcp_f32_e32 v109, v109
	v_add_f32_e32 v110, 1.0, v110
	v_add_f32_e32 v111, 1.0, v111
	v_rcp_f32_e32 v110, v110
	v_rcp_f32_e32 v111, v111
	v_pk_mul_f32 v[100:101], v[100:101], v[108:109]
	v_add_u32_e32 v114, s12, v114
	v_pk_mul_f32 v[96:97], v[100:101], v[96:97]
	v_ashrrev_i32_e32 v115, 31, v114
	v_pk_mul_f32 v[100:101], v[96:97], v[148:149] op_sel_hi:[1,0]
	v_pk_mul_f32 v[96:97], v[102:103], v[110:111]
	v_lshlrev_b64 v[114:115], 9, v[114:115]
	v_pk_mul_f32 v[96:97], v[96:97], v[98:99]
	v_lshl_add_u64 v[114:115], s[14:15], 0, v[114:115]
	v_pk_mul_f32 v[104:105], v[104:105], v[148:149] op_sel_hi:[1,0]
	v_pk_mul_f32 v[106:107], v[106:107], v[148:149] op_sel_hi:[1,0]
	v_pk_mul_f32 v[102:103], v[96:97], v[148:149] op_sel_hi:[1,0]
	v_lshl_add_u64 v[108:109], v[114:115], 0, v[112:113]
	v_cvt_pk_bf16_f32 v96, v104, v105
	v_cvt_pk_bf16_f32 v97, v106, v107
	v_cvt_pk_bf16_f32 v98, v100, v101
	v_cvt_pk_bf16_f32 v99, v102, v103
	global_store_dwordx4 v[108:109], v[96:99], off
	v_mul_f32_e32 v100, 0xbfb8aa3b, v94
	v_mul_f32_e32 v101, 0xbfb8aa3b, v95
	v_mul_f32_e32 v98, 0xbfb8aa3b, v92
	v_mul_f32_e32 v99, 0xbfb8aa3b, v93
	v_exp_f32_e32 v98, v98
	v_exp_f32_e32 v99, v99
	v_exp_f32_e32 v100, v100
	v_exp_f32_e32 v101, v101
	v_add_f32_e32 v98, 1.0, v98
	v_add_f32_e32 v99, 1.0, v99
	v_rcp_f32_e32 v98, v98
	v_rcp_f32_e32 v99, v99
	v_add_f32_e32 v100, 1.0, v100
	v_add_f32_e32 v101, 1.0, v101
	v_rcp_f32_e32 v100, v100
	v_rcp_f32_e32 v101, v101
	v_pk_mul_f32 v[92:93], v[92:93], v[98:99]
	v_add_u32_e32 v96, s12, v157
	v_pk_mul_f32 v[88:89], v[92:93], v[88:89]
	v_pk_mul_f32 v[92:93], v[94:95], v[100:101]
	v_mul_f32_e32 v94, 0xbfb8aa3b, v86
	v_pk_mul_f32 v[90:91], v[92:93], v[90:91]
	v_mul_f32_e32 v92, 0xbfb8aa3b, v84
	v_mul_f32_e32 v93, 0xbfb8aa3b, v85
	v_exp_f32_e32 v92, v92
	v_exp_f32_e32 v93, v93
	v_mul_f32_e32 v95, 0xbfb8aa3b, v87
	v_exp_f32_e32 v94, v94
	v_exp_f32_e32 v95, v95
	v_add_f32_e32 v92, 1.0, v92
	v_add_f32_e32 v93, 1.0, v93
	v_rcp_f32_e32 v92, v92
	v_rcp_f32_e32 v93, v93
	v_add_f32_e32 v94, 1.0, v94
	v_add_f32_e32 v95, 1.0, v95
	v_rcp_f32_e32 v94, v94
	v_rcp_f32_e32 v95, v95
	v_pk_mul_f32 v[84:85], v[84:85], v[92:93]
	v_ashrrev_i32_e32 v97, 31, v96
	v_pk_mul_f32 v[80:81], v[84:85], v[80:81]
	v_lshlrev_b64 v[96:97], 9, v[96:97]
	v_pk_mul_f32 v[84:85], v[80:81], v[146:147] op_sel_hi:[1,0]
	v_pk_mul_f32 v[80:81], v[86:87], v[94:95]
	v_lshl_add_u64 v[96:97], s[14:15], 0, v[96:97]
	v_pk_mul_f32 v[80:81], v[80:81], v[82:83]
	v_pk_mul_f32 v[88:89], v[88:89], v[146:147] op_sel_hi:[1,0]
	v_pk_mul_f32 v[90:91], v[90:91], v[146:147] op_sel_hi:[1,0]
	v_pk_mul_f32 v[86:87], v[80:81], v[146:147] op_sel_hi:[1,0]
	v_lshl_add_u64 v[92:93], v[96:97], 0, v[112:113]
	v_cvt_pk_bf16_f32 v80, v88, v89
	v_cvt_pk_bf16_f32 v81, v90, v91
	v_cvt_pk_bf16_f32 v82, v84, v85
	v_cvt_pk_bf16_f32 v83, v86, v87
	global_store_dwordx4 v[92:93], v[80:83], off
	v_mul_f32_e32 v84, 0xbfb8aa3b, v78
	v_mul_f32_e32 v85, 0xbfb8aa3b, v79
	v_mul_f32_e32 v82, 0xbfb8aa3b, v76
	v_mul_f32_e32 v83, 0xbfb8aa3b, v77
	v_exp_f32_e32 v82, v82
	v_exp_f32_e32 v83, v83
	v_exp_f32_e32 v84, v84
	v_exp_f32_e32 v85, v85
	v_add_f32_e32 v82, 1.0, v82
	v_add_f32_e32 v83, 1.0, v83
	v_rcp_f32_e32 v82, v82
	v_rcp_f32_e32 v83, v83
	v_add_f32_e32 v84, 1.0, v84
	v_add_f32_e32 v85, 1.0, v85
	v_rcp_f32_e32 v84, v84
	v_rcp_f32_e32 v85, v85
	v_pk_mul_f32 v[76:77], v[76:77], v[82:83]
	v_add_u32_e32 v80, s12, v158
	v_pk_mul_f32 v[72:73], v[76:77], v[72:73]
	v_pk_mul_f32 v[76:77], v[78:79], v[84:85]
	v_mul_f32_e32 v78, 0xbfb8aa3b, v70
	v_pk_mul_f32 v[74:75], v[76:77], v[74:75]
	v_mul_f32_e32 v76, 0xbfb8aa3b, v68
	v_mul_f32_e32 v77, 0xbfb8aa3b, v69
	v_exp_f32_e32 v76, v76
	v_exp_f32_e32 v77, v77
	v_mul_f32_e32 v79, 0xbfb8aa3b, v71
	v_exp_f32_e32 v78, v78
	v_exp_f32_e32 v79, v79
	v_add_f32_e32 v76, 1.0, v76
	v_add_f32_e32 v77, 1.0, v77
	v_rcp_f32_e32 v76, v76
	v_rcp_f32_e32 v77, v77
	v_add_f32_e32 v78, 1.0, v78
	v_add_f32_e32 v79, 1.0, v79
; DI unsigned pk_bf16(float lo, float hi) { const f32x2 v = {lo, hi}; return __builtin_bit_cast(unsigned, __builtin_convertvector(v, bf16x2_t)); }
; DI float silu_mul(float g, float u) { return g * sigmoidf_(g) * u; }
;     DI void operator()(const f32x4 (&acc)[2][2][4][2], const Unit& u, int wr, int wc, int fr, int fq) const {
;     ...
;         for (int ai = 0; ai < 2; ++ai)
; #pragma unroll
;             for (int m = 0; m < 4; ++m) { const int row = u.orow + ai * 128 + wr * 64 + m * 16 + fr;
;                 bf16_t* rowp = ACT + (size_t)row * 256 + col0;
;                 float v[8];
; #pragma unroll
;                 for (int n = 0; n < 2; ++n)
; #pragma unroll
;                     for (int j = 0; j < 4; ++j) v[n * 4 + j] = silu_mul(acc[ai][0][m][n][j], acc[ai][1][m][n][j]) * w8[ai][m];
;                 u32x4 w; w.x = pk_bf16(v[0], v[1]); w.y = pk_bf16(v[2], v[3]); w.z = pk_bf16(v[4], v[5]); w.w = pk_bf16(v[6], v[7]);
;                 *(u32x4*)rowp = w; }
	v_rcp_f32_e32 v78, v78
	v_rcp_f32_e32 v79, v79
	v_pk_mul_f32 v[68:69], v[68:69], v[76:77]
	v_ashrrev_i32_e32 v81, 31, v80
	v_pk_mul_f32 v[64:65], v[68:69], v[64:65]
	v_lshlrev_b64 v[80:81], 9, v[80:81]
	v_pk_mul_f32 v[68:69], v[64:65], v[144:145] op_sel_hi:[1,0]
	v_pk_mul_f32 v[64:65], v[70:71], v[78:79]
	v_lshl_add_u64 v[80:81], s[14:15], 0, v[80:81]
	v_pk_mul_f32 v[64:65], v[64:65], v[66:67]
	v_pk_mul_f32 v[72:73], v[72:73], v[144:145] op_sel_hi:[1,0]
	v_pk_mul_f32 v[74:75], v[74:75], v[144:145] op_sel_hi:[1,0]
	v_pk_mul_f32 v[70:71], v[64:65], v[144:145] op_sel_hi:[1,0]
	v_lshl_add_u64 v[76:77], v[80:81], 0, v[112:113]
	v_cvt_pk_bf16_f32 v64, v72, v73
	v_cvt_pk_bf16_f32 v65, v74, v75
	v_cvt_pk_bf16_f32 v66, v68, v69
	v_cvt_pk_bf16_f32 v67, v70, v71
	global_store_dwordx4 v[76:77], v[64:67], off
	v_mul_f32_e32 v68, 0xbfb8aa3b, v62
	v_mul_f32_e32 v69, 0xbfb8aa3b, v63
	v_mul_f32_e32 v66, 0xbfb8aa3b, v60
	v_mul_f32_e32 v67, 0xbfb8aa3b, v61
	v_exp_f32_e32 v66, v66
	v_exp_f32_e32 v67, v67
	v_exp_f32_e32 v68, v68
	v_exp_f32_e32 v69, v69
	v_add_f32_e32 v66, 1.0, v66
	v_add_f32_e32 v67, 1.0, v67
	v_rcp_f32_e32 v66, v66
	v_rcp_f32_e32 v67, v67
	v_add_f32_e32 v68, 1.0, v68
	v_add_f32_e32 v69, 1.0, v69
	v_rcp_f32_e32 v68, v68
	v_rcp_f32_e32 v69, v69
	v_pk_mul_f32 v[60:61], v[60:61], v[66:67]
	v_add_u32_e32 v64, s12, v159
	v_pk_mul_f32 v[56:57], v[60:61], v[56:57]
	v_pk_mul_f32 v[60:61], v[62:63], v[68:69]
	v_mul_f32_e32 v62, 0xbfb8aa3b, v54
	v_pk_mul_f32 v[58:59], v[60:61], v[58:59]
	v_mul_f32_e32 v60, 0xbfb8aa3b, v52
	v_mul_f32_e32 v61, 0xbfb8aa3b, v53
	v_exp_f32_e32 v60, v60
	v_exp_f32_e32 v61, v61
	v_mul_f32_e32 v63, 0xbfb8aa3b, v55
	v_exp_f32_e32 v62, v62
	v_exp_f32_e32 v63, v63
	v_add_f32_e32 v60, 1.0, v60
	v_add_f32_e32 v61, 1.0, v61
	v_rcp_f32_e32 v60, v60
	v_rcp_f32_e32 v61, v61
	v_add_f32_e32 v62, 1.0, v62
	v_add_f32_e32 v63, 1.0, v63
	v_rcp_f32_e32 v62, v62
	v_rcp_f32_e32 v63, v63
	v_pk_mul_f32 v[52:53], v[52:53], v[60:61]
	v_ashrrev_i32_e32 v65, 31, v64
	v_pk_mul_f32 v[48:49], v[52:53], v[48:49]
	v_lshlrev_b64 v[64:65], 9, v[64:65]
	v_pk_mul_f32 v[52:53], v[48:49], v[142:143] op_sel_hi:[1,0]
	v_pk_mul_f32 v[48:49], v[54:55], v[62:63]
	v_lshl_add_u64 v[64:65], s[14:15], 0, v[64:65]
	v_pk_mul_f32 v[48:49], v[48:49], v[50:51]
	v_pk_mul_f32 v[56:57], v[56:57], v[142:143] op_sel_hi:[1,0]
	v_pk_mul_f32 v[58:59], v[58:59], v[142:143] op_sel_hi:[1,0]
	v_pk_mul_f32 v[54:55], v[48:49], v[142:143] op_sel_hi:[1,0]
	v_lshl_add_u64 v[60:61], v[64:65], 0, v[112:113]
	v_cvt_pk_bf16_f32 v48, v56, v57
	v_cvt_pk_bf16_f32 v49, v58, v59
	v_cvt_pk_bf16_f32 v50, v52, v53
	v_cvt_pk_bf16_f32 v51, v54, v55
	global_store_dwordx4 v[60:61], v[48:51], off
	v_mul_f32_e32 v52, 0xbfb8aa3b, v46
	v_mul_f32_e32 v53, 0xbfb8aa3b, v47
	v_mul_f32_e32 v50, 0xbfb8aa3b, v44
	v_mul_f32_e32 v51, 0xbfb8aa3b, v45
	v_exp_f32_e32 v50, v50
	v_exp_f32_e32 v51, v51
	v_exp_f32_e32 v52, v52
	v_exp_f32_e32 v53, v53
	v_add_f32_e32 v50, 1.0, v50
	v_add_f32_e32 v51, 1.0, v51
	v_rcp_f32_e32 v50, v50
	v_rcp_f32_e32 v51, v51
	v_add_f32_e32 v52, 1.0, v52
	v_add_f32_e32 v53, 1.0, v53
	v_rcp_f32_e32 v52, v52
	v_rcp_f32_e32 v53, v53
	v_pk_mul_f32 v[44:45], v[44:45], v[50:51]
	v_add_u32_e32 v48, s12, v160
	v_pk_mul_f32 v[40:41], v[44:45], v[40:41]
	v_pk_mul_f32 v[44:45], v[46:47], v[52:53]
	v_mul_f32_e32 v46, 0xbfb8aa3b, v38
	v_pk_mul_f32 v[42:43], v[44:45], v[42:43]
	v_mul_f32_e32 v44, 0xbfb8aa3b, v36
	v_mul_f32_e32 v45, 0xbfb8aa3b, v37
	v_exp_f32_e32 v44, v44
	v_exp_f32_e32 v45, v45
	v_mul_f32_e32 v47, 0xbfb8aa3b, v39
	v_exp_f32_e32 v46, v46
	v_exp_f32_e32 v47, v47
	v_add_f32_e32 v44, 1.0, v44
	v_add_f32_e32 v45, 1.0, v45
	v_rcp_f32_e32 v44, v44
	v_rcp_f32_e32 v45, v45
	v_add_f32_e32 v46, 1.0, v46
	v_add_f32_e32 v47, 1.0, v47
	v_rcp_f32_e32 v46, v46
	v_rcp_f32_e32 v47, v47
	v_pk_mul_f32 v[36:37], v[36:37], v[44:45]
	v_ashrrev_i32_e32 v49, 31, v48
	v_pk_mul_f32 v[32:33], v[36:37], v[32:33]
	v_lshlrev_b64 v[48:49], 9, v[48:49]
	v_pk_mul_f32 v[36:37], v[32:33], v[140:141] op_sel_hi:[1,0]
	v_pk_mul_f32 v[32:33], v[38:39], v[46:47]
	v_lshl_add_u64 v[48:49], s[14:15], 0, v[48:49]
	v_pk_mul_f32 v[32:33], v[32:33], v[34:35]
	v_pk_mul_f32 v[40:41], v[40:41], v[140:141] op_sel_hi:[1,0]
	v_pk_mul_f32 v[42:43], v[42:43], v[140:141] op_sel_hi:[1,0]
	v_pk_mul_f32 v[38:39], v[32:33], v[140:141] op_sel_hi:[1,0]
	v_lshl_add_u64 v[44:45], v[48:49], 0, v[112:113]
	v_cvt_pk_bf16_f32 v32, v40, v41
	v_cvt_pk_bf16_f32 v33, v42, v43
	v_cvt_pk_bf16_f32 v34, v36, v37
	v_cvt_pk_bf16_f32 v35, v38, v39
	global_store_dwordx4 v[44:45], v[32:35], off
	v_mul_f32_e32 v36, 0xbfb8aa3b, v30
	v_mul_f32_e32 v37, 0xbfb8aa3b, v31
	v_mul_f32_e32 v34, 0xbfb8aa3b, v28
	v_mul_f32_e32 v35, 0xbfb8aa3b, v29
	v_exp_f32_e32 v34, v34
	v_exp_f32_e32 v35, v35
	v_exp_f32_e32 v36, v36
	v_exp_f32_e32 v37, v37
	v_add_f32_e32 v34, 1.0, v34
	v_add_f32_e32 v35, 1.0, v35
	v_rcp_f32_e32 v34, v34
	v_rcp_f32_e32 v35, v35
	v_add_f32_e32 v36, 1.0, v36
	v_add_f32_e32 v37, 1.0, v37
	v_rcp_f32_e32 v36, v36
	v_rcp_f32_e32 v37, v37
; #define LAS __attribute__((address_space(3)))
; DI unsigned pk_bf16(float lo, float hi) { const f32x2 v = {lo, hi}; return __builtin_bit_cast(unsigned, __builtin_convertvector(v, bf16x2_t)); }
; DI float silu_mul(float g, float u) { return g * sigmoidf_(g) * u; }
;     DI void operator()(const f32x4 (&acc)[2][2][4][2], const Unit& u, int wr, int wc, int fr, int fq) const {
;     ...
;         for (int ai = 0; ai < 2; ++ai)
; #pragma unroll
;             for (int m = 0; m < 4; ++m) { const int row = u.orow + ai * 128 + wr * 64 + m * 16 + fr;
;                 bf16_t* rowp = ACT + (size_t)row * 256 + col0;
;                 float v[8];
; #pragma unroll
;                 for (int n = 0; n < 2; ++n)
; #pragma unroll
;                     for (int j = 0; j < 4; ++j) v[n * 4 + j] = silu_mul(acc[ai][0][m][n][j], acc[ai][1][m][n][j]) * w8[ai][m];
;                 u32x4 w; w.x = pk_bf16(v[0], v[1]); w.y = pk_bf16(v[2], v[3]); w.z = pk_bf16(v[4], v[5]); w.w = pk_bf16(v[6], v[7]);
;                 *(u32x4*)rowp = w; }
; DI void tr_tile(const float* src, int N, int k0, int n0, float scale, bf16_t* dst_row0  , int K, bf16_t* dst_lo, LAS bf16_t* T, int lane) {
;     ...
;     for (int it = 0; it < 8; ++it) {
;         const int n = it * 8 + (lane >> 3), kc = (lane & 7) * 8;
;         const u32x4 w = *(const LAS u32x4*)(T + n * 72 + kc);
;         *(u32x4*)(dst_row0 + (size_t)n * K + kc) = w;
;     }
	v_pk_mul_f32 v[28:29], v[28:29], v[34:35]
	v_add_u32_e32 v32, s12, v161
	v_pk_mul_f32 v[24:25], v[28:29], v[24:25]
	v_pk_mul_f32 v[28:29], v[30:31], v[36:37]
	v_mul_f32_e32 v30, 0xbfb8aa3b, v22
	v_pk_mul_f32 v[26:27], v[28:29], v[26:27]
	v_mul_f32_e32 v28, 0xbfb8aa3b, v20
	v_mul_f32_e32 v29, 0xbfb8aa3b, v21
	v_exp_f32_e32 v28, v28
	v_exp_f32_e32 v29, v29
	v_mul_f32_e32 v31, 0xbfb8aa3b, v23
	v_exp_f32_e32 v30, v30
	v_exp_f32_e32 v31, v31
	v_add_f32_e32 v28, 1.0, v28
	v_add_f32_e32 v29, 1.0, v29
	v_rcp_f32_e32 v28, v28
	v_rcp_f32_e32 v29, v29
	v_add_f32_e32 v30, 1.0, v30
	v_add_f32_e32 v31, 1.0, v31
	v_rcp_f32_e32 v30, v30
	v_rcp_f32_e32 v31, v31
	v_pk_mul_f32 v[20:21], v[20:21], v[28:29]
	v_ashrrev_i32_e32 v33, 31, v32
	v_pk_mul_f32 v[16:17], v[20:21], v[16:17]
	v_lshlrev_b64 v[32:33], 9, v[32:33]
	v_pk_mul_f32 v[20:21], v[16:17], v[138:139] op_sel_hi:[1,0]
	v_pk_mul_f32 v[16:17], v[22:23], v[30:31]
	v_lshl_add_u64 v[32:33], s[14:15], 0, v[32:33]
	v_pk_mul_f32 v[16:17], v[16:17], v[18:19]
	v_pk_mul_f32 v[24:25], v[24:25], v[138:139] op_sel_hi:[1,0]
	v_pk_mul_f32 v[26:27], v[26:27], v[138:139] op_sel_hi:[1,0]
	v_pk_mul_f32 v[22:23], v[16:17], v[138:139] op_sel_hi:[1,0]
	v_lshl_add_u64 v[28:29], v[32:33], 0, v[112:113]
	v_cvt_pk_bf16_f32 v16, v24, v25
	v_cvt_pk_bf16_f32 v17, v26, v27
	v_cvt_pk_bf16_f32 v18, v20, v21
	v_cvt_pk_bf16_f32 v19, v22, v23
	global_store_dwordx4 v[28:29], v[16:19], off
	v_mul_f32_e32 v20, 0xbfb8aa3b, v14
	v_mul_f32_e32 v21, 0xbfb8aa3b, v15
	v_mul_f32_e32 v18, 0xbfb8aa3b, v12
	v_mul_f32_e32 v19, 0xbfb8aa3b, v13
	v_exp_f32_e32 v18, v18
	v_exp_f32_e32 v19, v19
	v_exp_f32_e32 v20, v20
	v_exp_f32_e32 v21, v21
	v_add_f32_e32 v18, 1.0, v18
	v_add_f32_e32 v19, 1.0, v19
	v_rcp_f32_e32 v18, v18
	v_rcp_f32_e32 v19, v19
	v_add_f32_e32 v20, 1.0, v20
	v_add_f32_e32 v21, 1.0, v21
	v_rcp_f32_e32 v20, v20
	v_rcp_f32_e32 v21, v21
	v_pk_mul_f32 v[12:13], v[12:13], v[18:19]
	v_add_u32_e32 v16, s12, v162
	v_pk_mul_f32 v[8:9], v[12:13], v[8:9]
	v_pk_mul_f32 v[12:13], v[14:15], v[20:21]
	v_mul_f32_e32 v14, 0xbfb8aa3b, v6
	v_pk_mul_f32 v[10:11], v[12:13], v[10:11]
	v_mul_f32_e32 v12, 0xbfb8aa3b, v4
	v_mul_f32_e32 v13, 0xbfb8aa3b, v5
	v_exp_f32_e32 v12, v12
	v_exp_f32_e32 v13, v13
	v_mul_f32_e32 v15, 0xbfb8aa3b, v7
	v_exp_f32_e32 v14, v14
	v_exp_f32_e32 v15, v15
	v_add_f32_e32 v12, 1.0, v12
	v_add_f32_e32 v13, 1.0, v13
	v_rcp_f32_e32 v12, v12
	v_rcp_f32_e32 v13, v13
	v_add_f32_e32 v14, 1.0, v14
	v_add_f32_e32 v15, 1.0, v15
	v_rcp_f32_e32 v14, v14
	v_rcp_f32_e32 v15, v15
	v_pk_mul_f32 v[4:5], v[4:5], v[12:13]
	v_ashrrev_i32_e32 v17, 31, v16
	v_pk_mul_f32 v[0:1], v[4:5], v[0:1]
	v_lshlrev_b64 v[16:17], 9, v[16:17]
	v_pk_mul_f32 v[4:5], v[0:1], v[136:137] op_sel_hi:[1,0]
	v_pk_mul_f32 v[0:1], v[6:7], v[14:15]
	v_lshl_add_u64 v[16:17], s[14:15], 0, v[16:17]
	v_pk_mul_f32 v[0:1], v[0:1], v[2:3]
	v_pk_mul_f32 v[8:9], v[8:9], v[136:137] op_sel_hi:[1,0]
	v_pk_mul_f32 v[10:11], v[10:11], v[136:137] op_sel_hi:[1,0]
	v_pk_mul_f32 v[6:7], v[0:1], v[136:137] op_sel_hi:[1,0]
	v_lshl_add_u64 v[12:13], v[16:17], 0, v[112:113]
	v_cvt_pk_bf16_f32 v0, v8, v9
	v_cvt_pk_bf16_f32 v1, v10, v11
	v_cvt_pk_bf16_f32 v2, v4, v5
	v_cvt_pk_bf16_f32 v3, v6, v7
	s_cmp_eq_u32 s85, 0
	s_cbranch_scc1 .Lcv_st_done
	s_waitcnt vmcnt(7)
	v_cvt_pk_bf16_f32 v178, v178, v179
	v_cvt_pk_bf16_f32 v179, v180, v181
	v_cvt_pk_bf16_f32 v180, v182, v183
	v_cvt_pk_bf16_f32 v181, v184, v185
	v_cvt_pk_bf16_f32 v182, v186, v187
	v_cvt_pk_bf16_f32 v183, v188, v189
	v_cvt_pk_bf16_f32 v184, v190, v191
	v_cvt_pk_bf16_f32 v185, v192, v193
	v_cvt_pk_bf16_f32 v186, v194, v195
	v_cvt_pk_bf16_f32 v187, v196, v197
	v_cvt_pk_bf16_f32 v188, v198, v199
	v_cvt_pk_bf16_f32 v189, v200, v201
	v_cvt_pk_bf16_f32 v190, v202, v203
	v_cvt_pk_bf16_f32 v191, v204, v205
	v_cvt_pk_bf16_f32 v192, v206, v207
	v_cvt_pk_bf16_f32 v193, v208, v209
	v_cvt_pk_bf16_f32 v194, v210, v211
	v_cvt_pk_bf16_f32 v195, v212, v213
	v_cvt_pk_bf16_f32 v196, v214, v215
	v_cvt_pk_bf16_f32 v197, v216, v217
	v_cvt_pk_bf16_f32 v198, v218, v219
	v_cvt_pk_bf16_f32 v199, v220, v221
	v_cvt_pk_bf16_f32 v200, v222, v223
	v_cvt_pk_bf16_f32 v201, v236, v237
	v_cvt_pk_bf16_f32 v202, v238, v239
	v_cvt_pk_bf16_f32 v203, v240, v241
	v_cvt_pk_bf16_f32 v204, v242, v243
	v_cvt_pk_bf16_f32 v205, v244, v245
	v_cvt_pk_bf16_f32 v206, v246, v247
	v_cvt_pk_bf16_f32 v207, v248, v249
	v_cvt_pk_bf16_f32 v208, v250, v251
	v_cvt_pk_bf16_f32 v209, v252, v253
	s_lshl_b32 s76, s85, 4
	global_store_dwordx4 v175, v[178:181], s[98:99] nt
	global_store_dwordx4 v175, v[194:197], s[98:99] offset:64 nt
	s_add_u32 s98, s98, s76
	s_addc_u32 s99, s99, 0
	global_store_dwordx4 v175, v[182:185], s[98:99] nt
	global_store_dwordx4 v175, v[198:201], s[98:99] offset:64 nt
	s_add_u32 s98, s98, s76
	s_addc_u32 s99, s99, 0
	global_store_dwordx4 v175, v[186:189], s[98:99] nt
	global_store_dwordx4 v175, v[202:205], s[98:99] offset:64 nt
	s_add_u32 s98, s98, s76
	s_addc_u32 s99, s99, 0
	global_store_dwordx4 v175, v[190:193], s[98:99] nt
	global_store_dwordx4 v175, v[206:209], s[98:99] offset:64 nt
